# e1_epi
# speedup vs baseline: 1.0128x; 1.0128x over previous
.LBB2_4:
	s_mul_i32 s8, s3, 0x7000
	s_add_i32 s8, s8, 0
	s_add_i32 s9, s8, s6
	v_add3_u32 v101, s9, v100, v98
	s_barrier
	ds_read_b128 v[104:107], v101 offset:12288
	ds_read_b128 v[108:111], v101 offset:13312
	ds_read_b128 v[112:115], v101 offset:14336
	ds_read_b128 v[116:119], v101 offset:15360
	v_add3_u32 v101, s8, v99, v98
	ds_read_b128 v[122:125], v101
	ds_read_b128 v[126:129], v101 offset:1024
	ds_read_b128 v[130:133], v101 offset:2048
	ds_read_b128 v[134:137], v101 offset:3072
	ds_read_b128 v[138:141], v101 offset:4096
	ds_read_b128 v[142:145], v101 offset:5120
	s_waitcnt lgkmcnt(0)
	v_mfma_f32_16x16x32_f16 v[94:97], v[122:125], v[104:107], v[94:97]
	s_add_i32 s8, s3, 1
	s_cmp_lg_u32 s3, 4
	s_cselect_b32 s3, s8, 0
	v_mfma_f32_16x16x32_f16 v[70:73], v[122:125], v[108:111], v[70:73]
	s_add_i32 s7, s7, -1
	s_cmp_eq_u32 s7, 0
	v_mfma_f32_16x16x32_f16 v[46:49], v[122:125], v[112:115], v[46:49]
	v_mfma_f32_16x16x32_f16 v[22:25], v[122:125], v[116:119], v[22:25]
	v_mfma_f32_16x16x32_f16 v[90:93], v[126:129], v[104:107], v[90:93]
	v_mfma_f32_16x16x32_f16 v[66:69], v[126:129], v[108:111], v[66:69]
	v_mfma_f32_16x16x32_f16 v[42:45], v[126:129], v[112:115], v[42:45]
	v_mfma_f32_16x16x32_f16 v[18:21], v[126:129], v[116:119], v[18:21]
	v_mfma_f32_16x16x32_f16 v[86:89], v[130:133], v[104:107], v[86:89]
	v_mfma_f32_16x16x32_f16 v[54:57], v[130:133], v[108:111], v[54:57]
	v_mfma_f32_16x16x32_f16 v[26:29], v[130:133], v[112:115], v[26:29]
	v_mfma_f32_16x16x32_f16 v[6:9], v[130:133], v[116:119], v[6:9]
	v_mfma_f32_16x16x32_f16 v[74:77], v[134:137], v[104:107], v[74:77]
	v_mfma_f32_16x16x32_f16 v[50:53], v[134:137], v[108:111], v[50:53]
	v_mfma_f32_16x16x32_f16 v[38:41], v[134:137], v[112:115], v[38:41]
	v_mfma_f32_16x16x32_f16 v[14:17], v[134:137], v[116:119], v[14:17]
	v_mfma_f32_16x16x32_f16 v[82:85], v[138:141], v[104:107], v[82:85]
	v_mfma_f32_16x16x32_f16 v[58:61], v[138:141], v[108:111], v[58:61]
	v_mfma_f32_16x16x32_f16 v[30:33], v[138:141], v[112:115], v[30:33]
	v_mfma_f32_16x16x32_f16 v[10:13], v[138:141], v[116:119], v[10:13]
	v_mfma_f32_16x16x32_f16 v[78:81], v[142:145], v[104:107], v[78:81]
	v_mfma_f32_16x16x32_f16 v[62:65], v[142:145], v[108:111], v[62:65]
	v_mfma_f32_16x16x32_f16 v[34:37], v[142:145], v[112:115], v[34:37]
	v_mfma_f32_16x16x32_f16 v[2:5], v[142:145], v[116:119], v[2:5]
	s_cbranch_scc0 .LBB2_4
	s_barrier
	s_mul_i32 s24, s22, 0x3400
	s_lshl_b32 s28, s2, 6
	s_add_i32 s29, s20, s28
	s_and_b32 s30, s29, 0x7ff
	v_add_u32_e32 v98, s30, v102
	v_lshlrev_b32_e32 v98, 8, v98
	v_lshl_add_u32 v98, v120, 4, v98
	v_add_u32_e32 v99, 0x1000, v98
	v_add_u32_e32 v100, 0x2000, v98
	v_add_u32_e32 v101, 0x3000, v98
	v_mul_u32_u24_e32 v103, 0xd0, v102
	v_lshl_add_u32 v103, v120, 3, v103
	v_add_u32_e32 v103, s24, v103
	v_lshrrev_b32_e32 v0, 2, v1
	v_and_b32_e32 v1, 3, v1
	v_mul_u32_u24_e32 v102, 0xd0, v0
	v_lshl_add_u32 v102, v1, 4, v102
	v_add_u32_e32 v102, s24, v102
	v_lshlrev_b32_e32 v0, 11, v0
	v_lshl_add_u32 v0, v1, 4, v0
	s_lshl_b32 s31, s5, 7
	s_add_i32 s35, s31, 0
	s_and_b32 s35, s35, 0xff
	s_add_u32 s36, s12, s35
	s_addc_u32 s37, s13, 0
	s_add_i32 s35, s31, 64
	s_and_b32 s35, s35, 0xff
	s_add_u32 s38, s12, s35
	s_addc_u32 s39, s13, 0
	s_add_i32 s35, s31, 128
	s_and_b32 s35, s35, 0xff
	s_add_u32 s40, s12, s35
	s_addc_u32 s41, s13, 0
	s_add_i32 s35, s31, 192
	s_and_b32 s35, s35, 0xff
	s_add_u32 s42, s12, s35
	s_addc_u32 s43, s13, 0
	global_load_dwordx4 v[104:107], v98, s[36:37]
	global_load_dwordx4 v[108:111], v98, s[38:39]
	global_load_dwordx4 v[112:115], v98, s[40:41]
	global_load_dwordx4 v[116:119], v98, s[42:43]
	global_load_dwordx4 v[120:123], v99, s[36:37]
	global_load_dwordx4 v[124:127], v99, s[38:39]
	global_load_dwordx4 v[128:131], v99, s[40:41]
	global_load_dwordx4 v[132:135], v99, s[42:43]
	global_load_dwordx4 v[136:139], v100, s[36:37]
	global_load_dwordx4 v[140:143], v100, s[38:39]
	global_load_dwordx4 v[144:147], v100, s[40:41]
	global_load_dwordx4 v[148:151], v100, s[42:43]
	global_load_dwordx4 v[152:155], v101, s[36:37]
	global_load_dwordx4 v[156:159], v101, s[38:39]
	global_load_dwordx4 v[160:163], v101, s[40:41]
	global_load_dwordx4 v[164:167], v101, s[42:43]
	s_add_i32 s34, s25, s23
	s_sub_i32 s32, 0x400, s34
	s_ashr_i32 s32, s32, 4
	s_max_i32 s32, s32, 0
	s_min_i32 s32, s32, 6
	s_sub_i32 s33, 0x800, s34
	s_ashr_i32 s33, s33, 4
	s_max_i32 s33, s33, 0
	s_min_i32 s33, s33, 6
	s_cmp_le_u32 s33, 5
	s_cbranch_scc1 .Lepi_v5
	s_waitcnt vmcnt(0)
	s_cmp_lg_u32 s32, 6
	s_cbranch_scc1 .Lepi_r5
	v_mul_f32_e32 v104, 0x3e38aa3b, v104
	v_mul_f32_e32 v105, 0x3e38aa3b, v105
	v_mul_f32_e32 v106, 0x3e38aa3b, v106
	v_mul_f32_e32 v107, 0x3e38aa3b, v107
	v_mul_f32_e32 v108, 0x3e38aa3b, v108
	v_mul_f32_e32 v109, 0x3e38aa3b, v109
	v_mul_f32_e32 v110, 0x3e38aa3b, v110
	v_mul_f32_e32 v111, 0x3e38aa3b, v111
	v_mul_f32_e32 v112, 0x3e38aa3b, v112
	v_mul_f32_e32 v113, 0x3e38aa3b, v113
	v_mul_f32_e32 v114, 0x3e38aa3b, v114
	v_mul_f32_e32 v115, 0x3e38aa3b, v115
	v_mul_f32_e32 v116, 0x3e38aa3b, v116
	v_mul_f32_e32 v117, 0x3e38aa3b, v117
	v_mul_f32_e32 v118, 0x3e38aa3b, v118
	v_mul_f32_e32 v119, 0x3e38aa3b, v119
	v_mul_f32_e32 v120, 0x3e38aa3b, v120
	v_mul_f32_e32 v121, 0x3e38aa3b, v121
	v_mul_f32_e32 v122, 0x3e38aa3b, v122
	v_mul_f32_e32 v123, 0x3e38aa3b, v123
	v_mul_f32_e32 v124, 0x3e38aa3b, v124
	v_mul_f32_e32 v125, 0x3e38aa3b, v125
	v_mul_f32_e32 v126, 0x3e38aa3b, v126
	v_mul_f32_e32 v127, 0x3e38aa3b, v127
	v_mul_f32_e32 v128, 0x3e38aa3b, v128
	v_mul_f32_e32 v129, 0x3e38aa3b, v129
	v_mul_f32_e32 v130, 0x3e38aa3b, v130
	v_mul_f32_e32 v131, 0x3e38aa3b, v131
	v_mul_f32_e32 v132, 0x3e38aa3b, v132
	v_mul_f32_e32 v133, 0x3e38aa3b, v133
	v_mul_f32_e32 v134, 0x3e38aa3b, v134
	v_mul_f32_e32 v135, 0x3e38aa3b, v135
	v_mul_f32_e32 v136, 0x3e38aa3b, v136
	v_mul_f32_e32 v137, 0x3e38aa3b, v137
	v_mul_f32_e32 v138, 0x3e38aa3b, v138
	v_mul_f32_e32 v139, 0x3e38aa3b, v139
	v_mul_f32_e32 v140, 0x3e38aa3b, v140
	v_mul_f32_e32 v141, 0x3e38aa3b, v141
	v_mul_f32_e32 v142, 0x3e38aa3b, v142
	v_mul_f32_e32 v143, 0x3e38aa3b, v143
	v_mul_f32_e32 v144, 0x3e38aa3b, v144
	v_mul_f32_e32 v145, 0x3e38aa3b, v145
	v_mul_f32_e32 v146, 0x3e38aa3b, v146
	v_mul_f32_e32 v147, 0x3e38aa3b, v147
	v_mul_f32_e32 v148, 0x3e38aa3b, v148
	v_mul_f32_e32 v149, 0x3e38aa3b, v149
	v_mul_f32_e32 v150, 0x3e38aa3b, v150
	v_mul_f32_e32 v151, 0x3e38aa3b, v151
	v_mul_f32_e32 v152, 0x3e38aa3b, v152
	v_mul_f32_e32 v153, 0x3e38aa3b, v153
	v_mul_f32_e32 v154, 0x3e38aa3b, v154
	v_mul_f32_e32 v155, 0x3e38aa3b, v155
	v_mul_f32_e32 v156, 0x3e38aa3b, v156
	v_mul_f32_e32 v157, 0x3e38aa3b, v157
	v_mul_f32_e32 v158, 0x3e38aa3b, v158
	v_mul_f32_e32 v159, 0x3e38aa3b, v159
	v_mul_f32_e32 v160, 0x3e38aa3b, v160
	v_mul_f32_e32 v161, 0x3e38aa3b, v161
	v_mul_f32_e32 v162, 0x3e38aa3b, v162
	v_mul_f32_e32 v163, 0x3e38aa3b, v163
	v_mul_f32_e32 v164, 0x3e38aa3b, v164
	v_mul_f32_e32 v165, 0x3e38aa3b, v165
	v_mul_f32_e32 v166, 0x3e38aa3b, v166
	v_mul_f32_e32 v167, 0x3e38aa3b, v167
.Lepi_r5:
	v_mul_f32_e32 v98, v79, v109
	v_mul_f32_e32 v99, v81, v111
	v_mul_f32_e32 v79, v79, v108
	v_mul_f32_e32 v81, v81, v110
	v_fma_f32 v79, v78, v109, v79
	v_fma_f32 v81, v80, v111, v81
	v_fma_f32 v78, v78, v108, -v98
	v_fma_f32 v80, v80, v110, -v99
	v_cvt_pk_f16_f32 v78, v78, v79
	v_cvt_pk_f16_f32 v79, v80, v81
	ds_write_b64 v103, v[78:79] offset:160
	v_mul_f32_e32 v98, v63, v125
	v_mul_f32_e32 v99, v65, v127
	v_mul_f32_e32 v63, v63, v124
	v_mul_f32_e32 v65, v65, v126
	v_fma_f32 v63, v62, v125, v63
	v_fma_f32 v65, v64, v127, v65
	v_fma_f32 v62, v62, v124, -v98
	v_fma_f32 v64, v64, v126, -v99
	v_cvt_pk_f16_f32 v62, v62, v63
	v_cvt_pk_f16_f32 v63, v64, v65
	ds_write_b64 v103, v[62:63] offset:3488
	v_mul_f32_e32 v98, v35, v141
	v_mul_f32_e32 v99, v37, v143
	v_mul_f32_e32 v35, v35, v140
	v_mul_f32_e32 v37, v37, v142
	v_fma_f32 v35, v34, v141, v35
	v_fma_f32 v37, v36, v143, v37
	v_fma_f32 v34, v34, v140, -v98
	v_fma_f32 v36, v36, v142, -v99
	v_cvt_pk_f16_f32 v34, v34, v35
	v_cvt_pk_f16_f32 v35, v36, v37
	ds_write_b64 v103, v[34:35] offset:6816
	v_mul_f32_e32 v98, v3, v157
	v_mul_f32_e32 v99, v5, v159
	v_mul_f32_e32 v3, v3, v156
	v_mul_f32_e32 v5, v5, v158
	v_fma_f32 v3, v2, v157, v3
	v_fma_f32 v5, v4, v159, v5
	v_fma_f32 v2, v2, v156, -v98
	v_fma_f32 v4, v4, v158, -v99
	v_cvt_pk_f16_f32 v2, v2, v3
	v_cvt_pk_f16_f32 v3, v4, v5
	ds_write_b64 v103, v[2:3] offset:10144
	s_branch .Lepi_d5
.Lepi_v5:
	v_cvt_pk_f16_f32 v78, v78, v79
	v_cvt_pk_f16_f32 v79, v80, v81
	ds_write_b64 v103, v[78:79] offset:160
	v_cvt_pk_f16_f32 v62, v62, v63
	v_cvt_pk_f16_f32 v63, v64, v65
	ds_write_b64 v103, v[62:63] offset:3488
	v_cvt_pk_f16_f32 v34, v34, v35
	v_cvt_pk_f16_f32 v35, v36, v37
	ds_write_b64 v103, v[34:35] offset:6816
	v_cvt_pk_f16_f32 v2, v2, v3
	v_cvt_pk_f16_f32 v3, v4, v5
	ds_write_b64 v103, v[2:3] offset:10144
.Lepi_d5:
	s_cmp_le_u32 s33, 4
	s_cbranch_scc1 .Lepi_v4
	s_waitcnt vmcnt(0)
	s_cmp_lg_u32 s32, 5
	s_cbranch_scc1 .Lepi_r4
	v_mul_f32_e32 v104, 0x3e38aa3b, v104
	v_mul_f32_e32 v105, 0x3e38aa3b, v105
	v_mul_f32_e32 v106, 0x3e38aa3b, v106
	v_mul_f32_e32 v107, 0x3e38aa3b, v107
	v_mul_f32_e32 v108, 0x3e38aa3b, v108
	v_mul_f32_e32 v109, 0x3e38aa3b, v109
	v_mul_f32_e32 v110, 0x3e38aa3b, v110
	v_mul_f32_e32 v111, 0x3e38aa3b, v111
	v_mul_f32_e32 v112, 0x3e38aa3b, v112
	v_mul_f32_e32 v113, 0x3e38aa3b, v113
	v_mul_f32_e32 v114, 0x3e38aa3b, v114
	v_mul_f32_e32 v115, 0x3e38aa3b, v115
	v_mul_f32_e32 v116, 0x3e38aa3b, v116
	v_mul_f32_e32 v117, 0x3e38aa3b, v117
	v_mul_f32_e32 v118, 0x3e38aa3b, v118
	v_mul_f32_e32 v119, 0x3e38aa3b, v119
	v_mul_f32_e32 v120, 0x3e38aa3b, v120
	v_mul_f32_e32 v121, 0x3e38aa3b, v121
	v_mul_f32_e32 v122, 0x3e38aa3b, v122
	v_mul_f32_e32 v123, 0x3e38aa3b, v123
	v_mul_f32_e32 v124, 0x3e38aa3b, v124
	v_mul_f32_e32 v125, 0x3e38aa3b, v125
	v_mul_f32_e32 v126, 0x3e38aa3b, v126
	v_mul_f32_e32 v127, 0x3e38aa3b, v127
	v_mul_f32_e32 v128, 0x3e38aa3b, v128
	v_mul_f32_e32 v129, 0x3e38aa3b, v129
	v_mul_f32_e32 v130, 0x3e38aa3b, v130
	v_mul_f32_e32 v131, 0x3e38aa3b, v131
	v_mul_f32_e32 v132, 0x3e38aa3b, v132
	v_mul_f32_e32 v133, 0x3e38aa3b, v133
	v_mul_f32_e32 v134, 0x3e38aa3b, v134
	v_mul_f32_e32 v135, 0x3e38aa3b, v135
	v_mul_f32_e32 v136, 0x3e38aa3b, v136
	v_mul_f32_e32 v137, 0x3e38aa3b, v137
	v_mul_f32_e32 v138, 0x3e38aa3b, v138
	v_mul_f32_e32 v139, 0x3e38aa3b, v139
	v_mul_f32_e32 v140, 0x3e38aa3b, v140
	v_mul_f32_e32 v141, 0x3e38aa3b, v141
	v_mul_f32_e32 v142, 0x3e38aa3b, v142
	v_mul_f32_e32 v143, 0x3e38aa3b, v143
	v_mul_f32_e32 v144, 0x3e38aa3b, v144
	v_mul_f32_e32 v145, 0x3e38aa3b, v145
	v_mul_f32_e32 v146, 0x3e38aa3b, v146
	v_mul_f32_e32 v147, 0x3e38aa3b, v147
	v_mul_f32_e32 v148, 0x3e38aa3b, v148
	v_mul_f32_e32 v149, 0x3e38aa3b, v149
	v_mul_f32_e32 v150, 0x3e38aa3b, v150
	v_mul_f32_e32 v151, 0x3e38aa3b, v151
	v_mul_f32_e32 v152, 0x3e38aa3b, v152
	v_mul_f32_e32 v153, 0x3e38aa3b, v153
	v_mul_f32_e32 v154, 0x3e38aa3b, v154
	v_mul_f32_e32 v155, 0x3e38aa3b, v155
	v_mul_f32_e32 v156, 0x3e38aa3b, v156
	v_mul_f32_e32 v157, 0x3e38aa3b, v157
	v_mul_f32_e32 v158, 0x3e38aa3b, v158
	v_mul_f32_e32 v159, 0x3e38aa3b, v159
	v_mul_f32_e32 v160, 0x3e38aa3b, v160
	v_mul_f32_e32 v161, 0x3e38aa3b, v161
	v_mul_f32_e32 v162, 0x3e38aa3b, v162
	v_mul_f32_e32 v163, 0x3e38aa3b, v163
	v_mul_f32_e32 v164, 0x3e38aa3b, v164
	v_mul_f32_e32 v165, 0x3e38aa3b, v165
	v_mul_f32_e32 v166, 0x3e38aa3b, v166
	v_mul_f32_e32 v167, 0x3e38aa3b, v167
.Lepi_r4:
	v_mul_f32_e32 v98, v83, v105
	v_mul_f32_e32 v99, v85, v107
	v_mul_f32_e32 v83, v83, v104
	v_mul_f32_e32 v85, v85, v106
	v_fma_f32 v83, v82, v105, v83
	v_fma_f32 v85, v84, v107, v85
	v_fma_f32 v82, v82, v104, -v98
	v_fma_f32 v84, v84, v106, -v99
	v_cvt_pk_f16_f32 v82, v82, v83
	v_cvt_pk_f16_f32 v83, v84, v85
	ds_write_b64 v103, v[82:83] offset:128
	v_mul_f32_e32 v98, v59, v121
	v_mul_f32_e32 v99, v61, v123
	v_mul_f32_e32 v59, v59, v120
	v_mul_f32_e32 v61, v61, v122
	v_fma_f32 v59, v58, v121, v59
	v_fma_f32 v61, v60, v123, v61
	v_fma_f32 v58, v58, v120, -v98
	v_fma_f32 v60, v60, v122, -v99
	v_cvt_pk_f16_f32 v58, v58, v59
	v_cvt_pk_f16_f32 v59, v60, v61
	ds_write_b64 v103, v[58:59] offset:3456
	v_mul_f32_e32 v98, v31, v137
	v_mul_f32_e32 v99, v33, v139
	v_mul_f32_e32 v31, v31, v136
	v_mul_f32_e32 v33, v33, v138
	v_fma_f32 v31, v30, v137, v31
	v_fma_f32 v33, v32, v139, v33
	v_fma_f32 v30, v30, v136, -v98
	v_fma_f32 v32, v32, v138, -v99
	v_cvt_pk_f16_f32 v30, v30, v31
	v_cvt_pk_f16_f32 v31, v32, v33
	ds_write_b64 v103, v[30:31] offset:6784
	v_mul_f32_e32 v98, v11, v153
	v_mul_f32_e32 v99, v13, v155
	v_mul_f32_e32 v11, v11, v152
	v_mul_f32_e32 v13, v13, v154
	v_fma_f32 v11, v10, v153, v11
	v_fma_f32 v13, v12, v155, v13
	v_fma_f32 v10, v10, v152, -v98
	v_fma_f32 v12, v12, v154, -v99
	v_cvt_pk_f16_f32 v10, v10, v11
	v_cvt_pk_f16_f32 v11, v12, v13
	ds_write_b64 v103, v[10:11] offset:10112
	s_branch .Lepi_d4
.Lepi_v4:
	v_cvt_pk_f16_f32 v82, v82, v83
	v_cvt_pk_f16_f32 v83, v84, v85
	ds_write_b64 v103, v[82:83] offset:128
	v_cvt_pk_f16_f32 v58, v58, v59
	v_cvt_pk_f16_f32 v59, v60, v61
	ds_write_b64 v103, v[58:59] offset:3456
	v_cvt_pk_f16_f32 v30, v30, v31
	v_cvt_pk_f16_f32 v31, v32, v33
	ds_write_b64 v103, v[30:31] offset:6784
	v_cvt_pk_f16_f32 v10, v10, v11
	v_cvt_pk_f16_f32 v11, v12, v13
	ds_write_b64 v103, v[10:11] offset:10112
.Lepi_d4:
	s_cmp_le_u32 s33, 3
	s_cbranch_scc1 .Lepi_v3
	s_waitcnt vmcnt(0)
	s_cmp_lg_u32 s32, 4
	s_cbranch_scc1 .Lepi_r3
	v_mul_f32_e32 v104, 0x3e38aa3b, v104
	v_mul_f32_e32 v105, 0x3e38aa3b, v105
	v_mul_f32_e32 v106, 0x3e38aa3b, v106
	v_mul_f32_e32 v107, 0x3e38aa3b, v107
	v_mul_f32_e32 v108, 0x3e38aa3b, v108
	v_mul_f32_e32 v109, 0x3e38aa3b, v109
	v_mul_f32_e32 v110, 0x3e38aa3b, v110
	v_mul_f32_e32 v111, 0x3e38aa3b, v111
	v_mul_f32_e32 v112, 0x3e38aa3b, v112
	v_mul_f32_e32 v113, 0x3e38aa3b, v113
	v_mul_f32_e32 v114, 0x3e38aa3b, v114
	v_mul_f32_e32 v115, 0x3e38aa3b, v115
	v_mul_f32_e32 v116, 0x3e38aa3b, v116
	v_mul_f32_e32 v117, 0x3e38aa3b, v117
	v_mul_f32_e32 v118, 0x3e38aa3b, v118
	v_mul_f32_e32 v119, 0x3e38aa3b, v119
	v_mul_f32_e32 v120, 0x3e38aa3b, v120
	v_mul_f32_e32 v121, 0x3e38aa3b, v121
	v_mul_f32_e32 v122, 0x3e38aa3b, v122
	v_mul_f32_e32 v123, 0x3e38aa3b, v123
	v_mul_f32_e32 v124, 0x3e38aa3b, v124
	v_mul_f32_e32 v125, 0x3e38aa3b, v125
	v_mul_f32_e32 v126, 0x3e38aa3b, v126
	v_mul_f32_e32 v127, 0x3e38aa3b, v127
	v_mul_f32_e32 v128, 0x3e38aa3b, v128
	v_mul_f32_e32 v129, 0x3e38aa3b, v129
	v_mul_f32_e32 v130, 0x3e38aa3b, v130
	v_mul_f32_e32 v131, 0x3e38aa3b, v131
	v_mul_f32_e32 v132, 0x3e38aa3b, v132
	v_mul_f32_e32 v133, 0x3e38aa3b, v133
	v_mul_f32_e32 v134, 0x3e38aa3b, v134
	v_mul_f32_e32 v135, 0x3e38aa3b, v135
	v_mul_f32_e32 v136, 0x3e38aa3b, v136
	v_mul_f32_e32 v137, 0x3e38aa3b, v137
	v_mul_f32_e32 v138, 0x3e38aa3b, v138
	v_mul_f32_e32 v139, 0x3e38aa3b, v139
	v_mul_f32_e32 v140, 0x3e38aa3b, v140
	v_mul_f32_e32 v141, 0x3e38aa3b, v141
	v_mul_f32_e32 v142, 0x3e38aa3b, v142
	v_mul_f32_e32 v143, 0x3e38aa3b, v143
	v_mul_f32_e32 v144, 0x3e38aa3b, v144
	v_mul_f32_e32 v145, 0x3e38aa3b, v145
	v_mul_f32_e32 v146, 0x3e38aa3b, v146
	v_mul_f32_e32 v147, 0x3e38aa3b, v147
	v_mul_f32_e32 v148, 0x3e38aa3b, v148
	v_mul_f32_e32 v149, 0x3e38aa3b, v149
	v_mul_f32_e32 v150, 0x3e38aa3b, v150
	v_mul_f32_e32 v151, 0x3e38aa3b, v151
	v_mul_f32_e32 v152, 0x3e38aa3b, v152
	v_mul_f32_e32 v153, 0x3e38aa3b, v153
	v_mul_f32_e32 v154, 0x3e38aa3b, v154
	v_mul_f32_e32 v155, 0x3e38aa3b, v155
	v_mul_f32_e32 v156, 0x3e38aa3b, v156
	v_mul_f32_e32 v157, 0x3e38aa3b, v157
	v_mul_f32_e32 v158, 0x3e38aa3b, v158
	v_mul_f32_e32 v159, 0x3e38aa3b, v159
	v_mul_f32_e32 v160, 0x3e38aa3b, v160
	v_mul_f32_e32 v161, 0x3e38aa3b, v161
	v_mul_f32_e32 v162, 0x3e38aa3b, v162
	v_mul_f32_e32 v163, 0x3e38aa3b, v163
	v_mul_f32_e32 v164, 0x3e38aa3b, v164
	v_mul_f32_e32 v165, 0x3e38aa3b, v165
	v_mul_f32_e32 v166, 0x3e38aa3b, v166
	v_mul_f32_e32 v167, 0x3e38aa3b, v167
.Lepi_r3:
	v_mul_f32_e32 v98, v75, v117
	v_mul_f32_e32 v99, v77, v119
	v_mul_f32_e32 v75, v75, v116
	v_mul_f32_e32 v77, v77, v118
	v_fma_f32 v75, v74, v117, v75
	v_fma_f32 v77, v76, v119, v77
	v_fma_f32 v74, v74, v116, -v98
	v_fma_f32 v76, v76, v118, -v99
	v_cvt_pk_f16_f32 v74, v74, v75
	v_cvt_pk_f16_f32 v75, v76, v77
	ds_write_b64 v103, v[74:75] offset:96
	v_mul_f32_e32 v98, v51, v133
	v_mul_f32_e32 v99, v53, v135
	v_mul_f32_e32 v51, v51, v132
	v_mul_f32_e32 v53, v53, v134
	v_fma_f32 v51, v50, v133, v51
	v_fma_f32 v53, v52, v135, v53
	v_fma_f32 v50, v50, v132, -v98
	v_fma_f32 v52, v52, v134, -v99
	v_cvt_pk_f16_f32 v50, v50, v51
	v_cvt_pk_f16_f32 v51, v52, v53
	ds_write_b64 v103, v[50:51] offset:3424
	v_mul_f32_e32 v98, v39, v149
	v_mul_f32_e32 v99, v41, v151
	v_mul_f32_e32 v39, v39, v148
	v_mul_f32_e32 v41, v41, v150
	v_fma_f32 v39, v38, v149, v39
	v_fma_f32 v41, v40, v151, v41
	v_fma_f32 v38, v38, v148, -v98
	v_fma_f32 v40, v40, v150, -v99
	v_cvt_pk_f16_f32 v38, v38, v39
	v_cvt_pk_f16_f32 v39, v40, v41
	ds_write_b64 v103, v[38:39] offset:6752
	v_mul_f32_e32 v98, v15, v165
	v_mul_f32_e32 v99, v17, v167
	v_mul_f32_e32 v15, v15, v164
	v_mul_f32_e32 v17, v17, v166
	v_fma_f32 v15, v14, v165, v15
	v_fma_f32 v17, v16, v167, v17
	v_fma_f32 v14, v14, v164, -v98
	v_fma_f32 v16, v16, v166, -v99
	v_cvt_pk_f16_f32 v14, v14, v15
	v_cvt_pk_f16_f32 v15, v16, v17
	ds_write_b64 v103, v[14:15] offset:10080
	s_branch .Lepi_d3
.Lepi_v3:
	v_cvt_pk_f16_f32 v74, v74, v75
	v_cvt_pk_f16_f32 v75, v76, v77
	ds_write_b64 v103, v[74:75] offset:96
	v_cvt_pk_f16_f32 v50, v50, v51
	v_cvt_pk_f16_f32 v51, v52, v53
	ds_write_b64 v103, v[50:51] offset:3424
	v_cvt_pk_f16_f32 v38, v38, v39
	v_cvt_pk_f16_f32 v39, v40, v41
	ds_write_b64 v103, v[38:39] offset:6752
	v_cvt_pk_f16_f32 v14, v14, v15
	v_cvt_pk_f16_f32 v15, v16, v17
	ds_write_b64 v103, v[14:15] offset:10080
.Lepi_d3:
	s_cmp_le_u32 s33, 2
	s_cbranch_scc1 .Lepi_v2
	s_waitcnt vmcnt(0)
	s_cmp_lg_u32 s32, 3
	s_cbranch_scc1 .Lepi_r2
	v_mul_f32_e32 v104, 0x3e38aa3b, v104
	v_mul_f32_e32 v105, 0x3e38aa3b, v105
	v_mul_f32_e32 v106, 0x3e38aa3b, v106
	v_mul_f32_e32 v107, 0x3e38aa3b, v107
	v_mul_f32_e32 v108, 0x3e38aa3b, v108
	v_mul_f32_e32 v109, 0x3e38aa3b, v109
	v_mul_f32_e32 v110, 0x3e38aa3b, v110
	v_mul_f32_e32 v111, 0x3e38aa3b, v111
	v_mul_f32_e32 v112, 0x3e38aa3b, v112
	v_mul_f32_e32 v113, 0x3e38aa3b, v113
	v_mul_f32_e32 v114, 0x3e38aa3b, v114
	v_mul_f32_e32 v115, 0x3e38aa3b, v115
	v_mul_f32_e32 v116, 0x3e38aa3b, v116
	v_mul_f32_e32 v117, 0x3e38aa3b, v117
	v_mul_f32_e32 v118, 0x3e38aa3b, v118
	v_mul_f32_e32 v119, 0x3e38aa3b, v119
	v_mul_f32_e32 v120, 0x3e38aa3b, v120
	v_mul_f32_e32 v121, 0x3e38aa3b, v121
	v_mul_f32_e32 v122, 0x3e38aa3b, v122
	v_mul_f32_e32 v123, 0x3e38aa3b, v123
	v_mul_f32_e32 v124, 0x3e38aa3b, v124
	v_mul_f32_e32 v125, 0x3e38aa3b, v125
	v_mul_f32_e32 v126, 0x3e38aa3b, v126
	v_mul_f32_e32 v127, 0x3e38aa3b, v127
	v_mul_f32_e32 v128, 0x3e38aa3b, v128
	v_mul_f32_e32 v129, 0x3e38aa3b, v129
	v_mul_f32_e32 v130, 0x3e38aa3b, v130
	v_mul_f32_e32 v131, 0x3e38aa3b, v131
	v_mul_f32_e32 v132, 0x3e38aa3b, v132
	v_mul_f32_e32 v133, 0x3e38aa3b, v133
	v_mul_f32_e32 v134, 0x3e38aa3b, v134
	v_mul_f32_e32 v135, 0x3e38aa3b, v135
	v_mul_f32_e32 v136, 0x3e38aa3b, v136
	v_mul_f32_e32 v137, 0x3e38aa3b, v137
	v_mul_f32_e32 v138, 0x3e38aa3b, v138
	v_mul_f32_e32 v139, 0x3e38aa3b, v139
	v_mul_f32_e32 v140, 0x3e38aa3b, v140
	v_mul_f32_e32 v141, 0x3e38aa3b, v141
	v_mul_f32_e32 v142, 0x3e38aa3b, v142
	v_mul_f32_e32 v143, 0x3e38aa3b, v143
	v_mul_f32_e32 v144, 0x3e38aa3b, v144
	v_mul_f32_e32 v145, 0x3e38aa3b, v145
	v_mul_f32_e32 v146, 0x3e38aa3b, v146
	v_mul_f32_e32 v147, 0x3e38aa3b, v147
	v_mul_f32_e32 v148, 0x3e38aa3b, v148
	v_mul_f32_e32 v149, 0x3e38aa3b, v149
	v_mul_f32_e32 v150, 0x3e38aa3b, v150
	v_mul_f32_e32 v151, 0x3e38aa3b, v151
	v_mul_f32_e32 v152, 0x3e38aa3b, v152
	v_mul_f32_e32 v153, 0x3e38aa3b, v153
	v_mul_f32_e32 v154, 0x3e38aa3b, v154
	v_mul_f32_e32 v155, 0x3e38aa3b, v155
	v_mul_f32_e32 v156, 0x3e38aa3b, v156
	v_mul_f32_e32 v157, 0x3e38aa3b, v157
	v_mul_f32_e32 v158, 0x3e38aa3b, v158
	v_mul_f32_e32 v159, 0x3e38aa3b, v159
	v_mul_f32_e32 v160, 0x3e38aa3b, v160
	v_mul_f32_e32 v161, 0x3e38aa3b, v161
	v_mul_f32_e32 v162, 0x3e38aa3b, v162
	v_mul_f32_e32 v163, 0x3e38aa3b, v163
	v_mul_f32_e32 v164, 0x3e38aa3b, v164
	v_mul_f32_e32 v165, 0x3e38aa3b, v165
	v_mul_f32_e32 v166, 0x3e38aa3b, v166
	v_mul_f32_e32 v167, 0x3e38aa3b, v167
.Lepi_r2:
	v_mul_f32_e32 v98, v87, v113
	v_mul_f32_e32 v99, v89, v115
	v_mul_f32_e32 v87, v87, v112
	v_mul_f32_e32 v89, v89, v114
	v_fma_f32 v87, v86, v113, v87
	v_fma_f32 v89, v88, v115, v89
	v_fma_f32 v86, v86, v112, -v98
	v_fma_f32 v88, v88, v114, -v99
	v_cvt_pk_f16_f32 v86, v86, v87
	v_cvt_pk_f16_f32 v87, v88, v89
	ds_write_b64 v103, v[86:87] offset:64
	v_mul_f32_e32 v98, v55, v129
	v_mul_f32_e32 v99, v57, v131
	v_mul_f32_e32 v55, v55, v128
	v_mul_f32_e32 v57, v57, v130
	v_fma_f32 v55, v54, v129, v55
	v_fma_f32 v57, v56, v131, v57
	v_fma_f32 v54, v54, v128, -v98
	v_fma_f32 v56, v56, v130, -v99
	v_cvt_pk_f16_f32 v54, v54, v55
	v_cvt_pk_f16_f32 v55, v56, v57
	ds_write_b64 v103, v[54:55] offset:3392
	v_mul_f32_e32 v98, v27, v145
	v_mul_f32_e32 v99, v29, v147
	v_mul_f32_e32 v27, v27, v144
	v_mul_f32_e32 v29, v29, v146
	v_fma_f32 v27, v26, v145, v27
	v_fma_f32 v29, v28, v147, v29
	v_fma_f32 v26, v26, v144, -v98
	v_fma_f32 v28, v28, v146, -v99
	v_cvt_pk_f16_f32 v26, v26, v27
	v_cvt_pk_f16_f32 v27, v28, v29
	ds_write_b64 v103, v[26:27] offset:6720
	v_mul_f32_e32 v98, v7, v161
	v_mul_f32_e32 v99, v9, v163
	v_mul_f32_e32 v7, v7, v160
	v_mul_f32_e32 v9, v9, v162
	v_fma_f32 v7, v6, v161, v7
	v_fma_f32 v9, v8, v163, v9
	v_fma_f32 v6, v6, v160, -v98
	v_fma_f32 v8, v8, v162, -v99
	v_cvt_pk_f16_f32 v6, v6, v7
	v_cvt_pk_f16_f32 v7, v8, v9
	ds_write_b64 v103, v[6:7] offset:10048
	s_branch .Lepi_d2
.Lepi_v2:
	v_cvt_pk_f16_f32 v86, v86, v87
	v_cvt_pk_f16_f32 v87, v88, v89
	ds_write_b64 v103, v[86:87] offset:64
	v_cvt_pk_f16_f32 v54, v54, v55
	v_cvt_pk_f16_f32 v55, v56, v57
	ds_write_b64 v103, v[54:55] offset:3392
	v_cvt_pk_f16_f32 v26, v26, v27
	v_cvt_pk_f16_f32 v27, v28, v29
	ds_write_b64 v103, v[26:27] offset:6720
	v_cvt_pk_f16_f32 v6, v6, v7
	v_cvt_pk_f16_f32 v7, v8, v9
	ds_write_b64 v103, v[6:7] offset:10048
.Lepi_d2:
	s_cmp_le_u32 s33, 1
	s_cbranch_scc1 .Lepi_v1
	s_waitcnt vmcnt(0)
	s_cmp_lg_u32 s32, 2
	s_cbranch_scc1 .Lepi_r1
	v_mul_f32_e32 v104, 0x3e38aa3b, v104
	v_mul_f32_e32 v105, 0x3e38aa3b, v105
	v_mul_f32_e32 v106, 0x3e38aa3b, v106
	v_mul_f32_e32 v107, 0x3e38aa3b, v107
	v_mul_f32_e32 v108, 0x3e38aa3b, v108
	v_mul_f32_e32 v109, 0x3e38aa3b, v109
	v_mul_f32_e32 v110, 0x3e38aa3b, v110
	v_mul_f32_e32 v111, 0x3e38aa3b, v111
	v_mul_f32_e32 v112, 0x3e38aa3b, v112
	v_mul_f32_e32 v113, 0x3e38aa3b, v113
	v_mul_f32_e32 v114, 0x3e38aa3b, v114
	v_mul_f32_e32 v115, 0x3e38aa3b, v115
	v_mul_f32_e32 v116, 0x3e38aa3b, v116
	v_mul_f32_e32 v117, 0x3e38aa3b, v117
	v_mul_f32_e32 v118, 0x3e38aa3b, v118
	v_mul_f32_e32 v119, 0x3e38aa3b, v119
	v_mul_f32_e32 v120, 0x3e38aa3b, v120
	v_mul_f32_e32 v121, 0x3e38aa3b, v121
	v_mul_f32_e32 v122, 0x3e38aa3b, v122
	v_mul_f32_e32 v123, 0x3e38aa3b, v123
	v_mul_f32_e32 v124, 0x3e38aa3b, v124
	v_mul_f32_e32 v125, 0x3e38aa3b, v125
	v_mul_f32_e32 v126, 0x3e38aa3b, v126
	v_mul_f32_e32 v127, 0x3e38aa3b, v127
	v_mul_f32_e32 v128, 0x3e38aa3b, v128
	v_mul_f32_e32 v129, 0x3e38aa3b, v129
	v_mul_f32_e32 v130, 0x3e38aa3b, v130
	v_mul_f32_e32 v131, 0x3e38aa3b, v131
	v_mul_f32_e32 v132, 0x3e38aa3b, v132
	v_mul_f32_e32 v133, 0x3e38aa3b, v133
	v_mul_f32_e32 v134, 0x3e38aa3b, v134
	v_mul_f32_e32 v135, 0x3e38aa3b, v135
	v_mul_f32_e32 v136, 0x3e38aa3b, v136
	v_mul_f32_e32 v137, 0x3e38aa3b, v137
	v_mul_f32_e32 v138, 0x3e38aa3b, v138
	v_mul_f32_e32 v139, 0x3e38aa3b, v139
	v_mul_f32_e32 v140, 0x3e38aa3b, v140
	v_mul_f32_e32 v141, 0x3e38aa3b, v141
	v_mul_f32_e32 v142, 0x3e38aa3b, v142
	v_mul_f32_e32 v143, 0x3e38aa3b, v143
	v_mul_f32_e32 v144, 0x3e38aa3b, v144
	v_mul_f32_e32 v145, 0x3e38aa3b, v145
	v_mul_f32_e32 v146, 0x3e38aa3b, v146
	v_mul_f32_e32 v147, 0x3e38aa3b, v147
	v_mul_f32_e32 v148, 0x3e38aa3b, v148
	v_mul_f32_e32 v149, 0x3e38aa3b, v149
	v_mul_f32_e32 v150, 0x3e38aa3b, v150
	v_mul_f32_e32 v151, 0x3e38aa3b, v151
	v_mul_f32_e32 v152, 0x3e38aa3b, v152
	v_mul_f32_e32 v153, 0x3e38aa3b, v153
	v_mul_f32_e32 v154, 0x3e38aa3b, v154
	v_mul_f32_e32 v155, 0x3e38aa3b, v155
	v_mul_f32_e32 v156, 0x3e38aa3b, v156
	v_mul_f32_e32 v157, 0x3e38aa3b, v157
	v_mul_f32_e32 v158, 0x3e38aa3b, v158
	v_mul_f32_e32 v159, 0x3e38aa3b, v159
	v_mul_f32_e32 v160, 0x3e38aa3b, v160
	v_mul_f32_e32 v161, 0x3e38aa3b, v161
	v_mul_f32_e32 v162, 0x3e38aa3b, v162
	v_mul_f32_e32 v163, 0x3e38aa3b, v163
	v_mul_f32_e32 v164, 0x3e38aa3b, v164
	v_mul_f32_e32 v165, 0x3e38aa3b, v165
	v_mul_f32_e32 v166, 0x3e38aa3b, v166
	v_mul_f32_e32 v167, 0x3e38aa3b, v167
.Lepi_r1:
	v_mul_f32_e32 v98, v91, v109
	v_mul_f32_e32 v99, v93, v111
	v_mul_f32_e32 v91, v91, v108
	v_mul_f32_e32 v93, v93, v110
	v_fma_f32 v91, v90, v109, v91
	v_fma_f32 v93, v92, v111, v93
	v_fma_f32 v90, v90, v108, -v98
	v_fma_f32 v92, v92, v110, -v99
	v_cvt_pk_f16_f32 v90, v90, v91
	v_cvt_pk_f16_f32 v91, v92, v93
	ds_write_b64 v103, v[90:91] offset:32
	v_mul_f32_e32 v98, v67, v125
	v_mul_f32_e32 v99, v69, v127
	v_mul_f32_e32 v67, v67, v124
	v_mul_f32_e32 v69, v69, v126
	v_fma_f32 v67, v66, v125, v67
	v_fma_f32 v69, v68, v127, v69
	v_fma_f32 v66, v66, v124, -v98
	v_fma_f32 v68, v68, v126, -v99
	v_cvt_pk_f16_f32 v66, v66, v67
	v_cvt_pk_f16_f32 v67, v68, v69
	ds_write_b64 v103, v[66:67] offset:3360
	v_mul_f32_e32 v98, v43, v141
	v_mul_f32_e32 v99, v45, v143
	v_mul_f32_e32 v43, v43, v140
	v_mul_f32_e32 v45, v45, v142
	v_fma_f32 v43, v42, v141, v43
	v_fma_f32 v45, v44, v143, v45
	v_fma_f32 v42, v42, v140, -v98
	v_fma_f32 v44, v44, v142, -v99
	v_cvt_pk_f16_f32 v42, v42, v43
	v_cvt_pk_f16_f32 v43, v44, v45
	ds_write_b64 v103, v[42:43] offset:6688
	v_mul_f32_e32 v98, v19, v157
	v_mul_f32_e32 v99, v21, v159
	v_mul_f32_e32 v19, v19, v156
	v_mul_f32_e32 v21, v21, v158
	v_fma_f32 v19, v18, v157, v19
	v_fma_f32 v21, v20, v159, v21
	v_fma_f32 v18, v18, v156, -v98
	v_fma_f32 v20, v20, v158, -v99
	v_cvt_pk_f16_f32 v18, v18, v19
	v_cvt_pk_f16_f32 v19, v20, v21
	ds_write_b64 v103, v[18:19] offset:10016
	s_branch .Lepi_d1
.Lepi_v1:
	v_cvt_pk_f16_f32 v90, v90, v91
	v_cvt_pk_f16_f32 v91, v92, v93
	ds_write_b64 v103, v[90:91] offset:32
	v_cvt_pk_f16_f32 v66, v66, v67
	v_cvt_pk_f16_f32 v67, v68, v69
	ds_write_b64 v103, v[66:67] offset:3360
	v_cvt_pk_f16_f32 v42, v42, v43
	v_cvt_pk_f16_f32 v43, v44, v45
	ds_write_b64 v103, v[42:43] offset:6688
	v_cvt_pk_f16_f32 v18, v18, v19
	v_cvt_pk_f16_f32 v19, v20, v21
	ds_write_b64 v103, v[18:19] offset:10016
.Lepi_d1:
	s_cmp_le_u32 s33, 0
	s_cbranch_scc1 .Lepi_v0
	s_waitcnt vmcnt(0)
	s_cmp_lg_u32 s32, 1
	s_cbranch_scc1 .Lepi_r0
	v_mul_f32_e32 v104, 0x3e38aa3b, v104
	v_mul_f32_e32 v105, 0x3e38aa3b, v105
	v_mul_f32_e32 v106, 0x3e38aa3b, v106
	v_mul_f32_e32 v107, 0x3e38aa3b, v107
	v_mul_f32_e32 v108, 0x3e38aa3b, v108
	v_mul_f32_e32 v109, 0x3e38aa3b, v109
	v_mul_f32_e32 v110, 0x3e38aa3b, v110
	v_mul_f32_e32 v111, 0x3e38aa3b, v111
	v_mul_f32_e32 v112, 0x3e38aa3b, v112
	v_mul_f32_e32 v113, 0x3e38aa3b, v113
	v_mul_f32_e32 v114, 0x3e38aa3b, v114
	v_mul_f32_e32 v115, 0x3e38aa3b, v115
	v_mul_f32_e32 v116, 0x3e38aa3b, v116
	v_mul_f32_e32 v117, 0x3e38aa3b, v117
	v_mul_f32_e32 v118, 0x3e38aa3b, v118
	v_mul_f32_e32 v119, 0x3e38aa3b, v119
	v_mul_f32_e32 v120, 0x3e38aa3b, v120
	v_mul_f32_e32 v121, 0x3e38aa3b, v121
	v_mul_f32_e32 v122, 0x3e38aa3b, v122
	v_mul_f32_e32 v123, 0x3e38aa3b, v123
	v_mul_f32_e32 v124, 0x3e38aa3b, v124
	v_mul_f32_e32 v125, 0x3e38aa3b, v125
	v_mul_f32_e32 v126, 0x3e38aa3b, v126
	v_mul_f32_e32 v127, 0x3e38aa3b, v127
	v_mul_f32_e32 v128, 0x3e38aa3b, v128
	v_mul_f32_e32 v129, 0x3e38aa3b, v129
	v_mul_f32_e32 v130, 0x3e38aa3b, v130
	v_mul_f32_e32 v131, 0x3e38aa3b, v131
	v_mul_f32_e32 v132, 0x3e38aa3b, v132
	v_mul_f32_e32 v133, 0x3e38aa3b, v133
	v_mul_f32_e32 v134, 0x3e38aa3b, v134
	v_mul_f32_e32 v135, 0x3e38aa3b, v135
	v_mul_f32_e32 v136, 0x3e38aa3b, v136
	v_mul_f32_e32 v137, 0x3e38aa3b, v137
	v_mul_f32_e32 v138, 0x3e38aa3b, v138
	v_mul_f32_e32 v139, 0x3e38aa3b, v139
	v_mul_f32_e32 v140, 0x3e38aa3b, v140
	v_mul_f32_e32 v141, 0x3e38aa3b, v141
	v_mul_f32_e32 v142, 0x3e38aa3b, v142
	v_mul_f32_e32 v143, 0x3e38aa3b, v143
	v_mul_f32_e32 v144, 0x3e38aa3b, v144
	v_mul_f32_e32 v145, 0x3e38aa3b, v145
	v_mul_f32_e32 v146, 0x3e38aa3b, v146
	v_mul_f32_e32 v147, 0x3e38aa3b, v147
	v_mul_f32_e32 v148, 0x3e38aa3b, v148
	v_mul_f32_e32 v149, 0x3e38aa3b, v149
	v_mul_f32_e32 v150, 0x3e38aa3b, v150
	v_mul_f32_e32 v151, 0x3e38aa3b, v151
	v_mul_f32_e32 v152, 0x3e38aa3b, v152
	v_mul_f32_e32 v153, 0x3e38aa3b, v153
	v_mul_f32_e32 v154, 0x3e38aa3b, v154
	v_mul_f32_e32 v155, 0x3e38aa3b, v155
	v_mul_f32_e32 v156, 0x3e38aa3b, v156
	v_mul_f32_e32 v157, 0x3e38aa3b, v157
	v_mul_f32_e32 v158, 0x3e38aa3b, v158
	v_mul_f32_e32 v159, 0x3e38aa3b, v159
	v_mul_f32_e32 v160, 0x3e38aa3b, v160
	v_mul_f32_e32 v161, 0x3e38aa3b, v161
	v_mul_f32_e32 v162, 0x3e38aa3b, v162
	v_mul_f32_e32 v163, 0x3e38aa3b, v163
	v_mul_f32_e32 v164, 0x3e38aa3b, v164
	v_mul_f32_e32 v165, 0x3e38aa3b, v165
	v_mul_f32_e32 v166, 0x3e38aa3b, v166
	v_mul_f32_e32 v167, 0x3e38aa3b, v167
.Lepi_r0:
	v_mul_f32_e32 v98, v95, v105
	v_mul_f32_e32 v99, v97, v107
	v_mul_f32_e32 v95, v95, v104
	v_mul_f32_e32 v97, v97, v106
	v_fma_f32 v95, v94, v105, v95
	v_fma_f32 v97, v96, v107, v97
	v_fma_f32 v94, v94, v104, -v98
	v_fma_f32 v96, v96, v106, -v99
	v_cvt_pk_f16_f32 v94, v94, v95
	v_cvt_pk_f16_f32 v95, v96, v97
	ds_write_b64 v103, v[94:95] offset:0
	v_mul_f32_e32 v98, v71, v121
	v_mul_f32_e32 v99, v73, v123
	v_mul_f32_e32 v71, v71, v120
	v_mul_f32_e32 v73, v73, v122
	v_fma_f32 v71, v70, v121, v71
	v_fma_f32 v73, v72, v123, v73
	v_fma_f32 v70, v70, v120, -v98
	v_fma_f32 v72, v72, v122, -v99
	v_cvt_pk_f16_f32 v70, v70, v71
	v_cvt_pk_f16_f32 v71, v72, v73
	ds_write_b64 v103, v[70:71] offset:3328
	v_mul_f32_e32 v98, v47, v137
	v_mul_f32_e32 v99, v49, v139
	v_mul_f32_e32 v47, v47, v136
	v_mul_f32_e32 v49, v49, v138
	v_fma_f32 v47, v46, v137, v47
	v_fma_f32 v49, v48, v139, v49
	v_fma_f32 v46, v46, v136, -v98
	v_fma_f32 v48, v48, v138, -v99
	v_cvt_pk_f16_f32 v46, v46, v47
	v_cvt_pk_f16_f32 v47, v48, v49
	ds_write_b64 v103, v[46:47] offset:6656
	v_mul_f32_e32 v98, v23, v153
	v_mul_f32_e32 v99, v25, v155
	v_mul_f32_e32 v23, v23, v152
	v_mul_f32_e32 v25, v25, v154
	v_fma_f32 v23, v22, v153, v23
	v_fma_f32 v25, v24, v155, v25
	v_fma_f32 v22, v22, v152, -v98
	v_fma_f32 v24, v24, v154, -v99
	v_cvt_pk_f16_f32 v22, v22, v23
	v_cvt_pk_f16_f32 v23, v24, v25
	ds_write_b64 v103, v[22:23] offset:9984
	s_branch .Lepi_d0
.Lepi_v0:
	v_cvt_pk_f16_f32 v94, v94, v95
	v_cvt_pk_f16_f32 v95, v96, v97
	ds_write_b64 v103, v[94:95] offset:0
	v_cvt_pk_f16_f32 v70, v70, v71
	v_cvt_pk_f16_f32 v71, v72, v73
	ds_write_b64 v103, v[70:71] offset:3328
	v_cvt_pk_f16_f32 v46, v46, v47
	v_cvt_pk_f16_f32 v47, v48, v49
	ds_write_b64 v103, v[46:47] offset:6656
	v_cvt_pk_f16_f32 v22, v22, v23
	v_cvt_pk_f16_f32 v23, v24, v25
	ds_write_b64 v103, v[22:23] offset:9984
.Lepi_d0:
	s_waitcnt vmcnt(0)
	s_lshl_b32 s35, s29, 11
	v_add_u32_e32 v104, 0x8000, v0
	v_add_u32_e32 v105, 0x10000, v0
	v_add_u32_e32 v106, 0x18000, v0
	s_add_i32 s31, s34, 0
	s_lshr_b32 s30, s31, 10
	s_and_b32 s31, s31, 0x3ff
	s_lshl_b32 s31, s31, 1
	s_cmp_eq_u32 s30, 1
	s_cselect_b64 s[44:45], s[16:17], s[14:15]
	s_cmp_eq_u32 s30, 2
	s_cselect_b64 s[44:45], s[18:19], s[44:45]
	s_add_u32 s44, s44, s31
	s_addc_u32 s45, s45, 0
	s_add_u32 s44, s44, s35
	s_addc_u32 s45, s45, 0
	s_add_i32 s31, s34, 32
	s_lshr_b32 s30, s31, 10
	s_and_b32 s31, s31, 0x3ff
	s_lshl_b32 s31, s31, 1
	s_cmp_eq_u32 s30, 1
	s_cselect_b64 s[46:47], s[16:17], s[14:15]
	s_cmp_eq_u32 s30, 2
	s_cselect_b64 s[46:47], s[18:19], s[46:47]
	s_add_u32 s46, s46, s31
	s_addc_u32 s47, s47, 0
	s_add_u32 s46, s46, s35
	s_addc_u32 s47, s47, 0
	s_add_i32 s31, s34, 64
	s_lshr_b32 s30, s31, 10
	s_and_b32 s31, s31, 0x3ff
	s_lshl_b32 s31, s31, 1
	s_cmp_eq_u32 s30, 1
	s_cselect_b64 s[48:49], s[16:17], s[14:15]
	s_cmp_eq_u32 s30, 2
	s_cselect_b64 s[48:49], s[18:19], s[48:49]
	s_add_u32 s48, s48, s31
	s_addc_u32 s49, s49, 0
	s_add_u32 s48, s48, s35
	s_addc_u32 s49, s49, 0
	s_waitcnt lgkmcnt(0)
	ds_read_b128 v[2:5], v102 offset:0
	ds_read_b128 v[6:9], v102 offset:64
	ds_read_b128 v[10:13], v102 offset:128
	ds_read_b128 v[14:17], v102 offset:3328
	ds_read_b128 v[18:21], v102 offset:3392
	ds_read_b128 v[22:25], v102 offset:3456
	ds_read_b128 v[26:29], v102 offset:6656
	ds_read_b128 v[30:33], v102 offset:6720
	ds_read_b128 v[34:37], v102 offset:6784
	ds_read_b128 v[38:41], v102 offset:9984
	ds_read_b128 v[42:45], v102 offset:10048
	ds_read_b128 v[46:49], v102 offset:10112
	s_waitcnt lgkmcnt(11)
	global_store_dwordx4 v0, v[2:5], s[44:45]
	s_waitcnt lgkmcnt(10)
	global_store_dwordx4 v0, v[6:9], s[46:47]
	s_waitcnt lgkmcnt(9)
	global_store_dwordx4 v0, v[10:13], s[48:49]
	s_waitcnt lgkmcnt(8)
	global_store_dwordx4 v104, v[14:17], s[44:45]
	s_waitcnt lgkmcnt(7)
	global_store_dwordx4 v104, v[18:21], s[46:47]
	s_waitcnt lgkmcnt(6)
	global_store_dwordx4 v104, v[22:25], s[48:49]
	s_waitcnt lgkmcnt(5)
	global_store_dwordx4 v105, v[26:29], s[44:45]
	s_waitcnt lgkmcnt(4)
	global_store_dwordx4 v105, v[30:33], s[46:47]
	s_waitcnt lgkmcnt(3)
	global_store_dwordx4 v105, v[34:37], s[48:49]
	s_waitcnt lgkmcnt(2)
	global_store_dwordx4 v106, v[38:41], s[44:45]
	s_waitcnt lgkmcnt(1)
	global_store_dwordx4 v106, v[42:45], s[46:47]
	s_waitcnt lgkmcnt(0)
	global_store_dwordx4 v106, v[46:49], s[48:49]
	s_branch .LBB2_2
.LBB2_6:
	s_load_dwordx4 s[0:3], s[0:1], 0x0
	s_add_i32 s9, s22, -8
	s_mov_b32 s28, s23
	s_mov_b32 s29, s20
	v_and_b32_e32 v1, 63, v0
	v_bfe_u32 v3, v0, 4, 2
	v_lshrrev_b32_e32 v2, 2, v1
	v_sub_u32_e32 v3, 0, v3
	v_and_b32_e32 v3, 3, v3
	v_and_b32_e32 v4, 3, v1
	v_xor_b32_e32 v3, v3, v4
	v_lshlrev_b32_e32 v3, 4, v3
	v_lshl_or_b32 v2, v2, 6, v3
	s_lshl_b32 s4, s9, 4
	s_add_i32 s5, s28, s4
	s_lshl_b32 s5, s5, 6
	s_add_i32 s6, s29, s4
	s_lshl_b32 s6, s6, 6
	s_lshl_b32 s8, s9, 10
	s_waitcnt lgkmcnt(0)
	s_add_u32 s10, s0, s5
	s_addc_u32 s11, s1, 0
	s_add_u32 s12, s10, 0x1000
	s_addc_u32 s13, s11, 0
	s_add_u32 s14, s12, 0x1000
	s_addc_u32 s15, s13, 0
	s_add_u32 s16, s2, s6
	s_addc_u32 s17, s3, 0
	s_add_u32 s18, s16, 0x1000
	s_addc_u32 s19, s17, 0
	s_add_u32 s24, s18, 0x1000
	s_addc_u32 s25, s19, 0
	s_add_u32 s26, s24, 0x1000
	s_addc_u32 s27, s25, 0
	v_mov_b32_e32 v5, v2
	v_mov_b32_e32 v6, v2
	s_add_i32 m0, s8, 0
	s_nop 0
	global_load_lds_dwordx4 v5, s[10:11]
	s_add_i32 m0, s8, 4096
	s_nop 0
	global_load_lds_dwordx4 v5, s[12:13]
	s_add_i32 m0, s8, 8192
	s_nop 0
	global_load_lds_dwordx4 v5, s[14:15]
	s_add_i32 m0, s8, 12288
	s_nop 0
	global_load_lds_dwordx4 v6, s[16:17]
	s_add_i32 m0, s8, 16384
	s_nop 0
	global_load_lds_dwordx4 v6, s[18:19]
	s_add_i32 m0, s8, 20480
	s_nop 0
	global_load_lds_dwordx4 v6, s[24:25]
	s_add_i32 m0, s8, 24576
	s_nop 0
	global_load_lds_dwordx4 v6, s[26:27]
	v_add_u32_e32 v5, 196608, v5
	v_add_u32_e32 v6, 262144, v6
	s_add_i32 m0, s8, 28672
	s_nop 0
	global_load_lds_dwordx4 v5, s[10:11]
	s_add_i32 m0, s8, 32768
	s_nop 0
	global_load_lds_dwordx4 v5, s[12:13]
	s_add_i32 m0, s8, 36864
	s_nop 0
	global_load_lds_dwordx4 v5, s[14:15]
	s_add_i32 m0, s8, 40960
	s_nop 0
	global_load_lds_dwordx4 v6, s[16:17]
	s_add_i32 m0, s8, 45056
	s_nop 0
	global_load_lds_dwordx4 v6, s[18:19]
	s_add_i32 m0, s8, 49152
	s_nop 0
	global_load_lds_dwordx4 v6, s[24:25]
	s_add_i32 m0, s8, 53248
	s_nop 0
	global_load_lds_dwordx4 v6, s[26:27]
	v_add_u32_e32 v5, 196608, v5
	v_add_u32_e32 v6, 262144, v6
	s_add_i32 m0, s8, 57344
	s_nop 0
	global_load_lds_dwordx4 v5, s[10:11]
	s_add_i32 m0, s8, 61440
	s_nop 0
	global_load_lds_dwordx4 v5, s[12:13]
	s_add_i32 m0, s8, 65536
	s_nop 0
	global_load_lds_dwordx4 v5, s[14:15]
	s_add_i32 m0, s8, 69632
	s_nop 0
	global_load_lds_dwordx4 v6, s[16:17]
	s_add_i32 m0, s8, 73728
	s_nop 0
	global_load_lds_dwordx4 v6, s[18:19]
	s_add_i32 m0, s8, 77824
	s_nop 0
	global_load_lds_dwordx4 v6, s[24:25]
	s_add_i32 m0, s8, 81920
	s_nop 0
	global_load_lds_dwordx4 v6, s[26:27]
	v_add_u32_e32 v5, 196608, v5
	v_add_u32_e32 v6, 262144, v6
	s_add_i32 m0, s8, 86016
	s_nop 0
	global_load_lds_dwordx4 v5, s[10:11]
	s_add_i32 m0, s8, 90112
	s_nop 0
	global_load_lds_dwordx4 v5, s[12:13]
	s_add_i32 m0, s8, 94208
	s_nop 0
	global_load_lds_dwordx4 v5, s[14:15]
	s_add_i32 m0, s8, 98304
	s_nop 0
	global_load_lds_dwordx4 v6, s[16:17]
	s_add_i32 m0, s8, 102400
	s_nop 0
	global_load_lds_dwordx4 v6, s[18:19]
	s_add_i32 m0, s8, 106496
	s_nop 0
	global_load_lds_dwordx4 v6, s[24:25]
	s_add_i32 m0, s8, 110592
	s_nop 0
	global_load_lds_dwordx4 v6, s[26:27]
	v_add_u32_e32 v5, 196608, v5
	v_add_u32_e32 v6, 262144, v6
	s_mov_b32 s29, 4
	s_mov_b32 s30, 28

	.amdhsa_kernel _Z11gemm_kernelILi0ELi6ELi4ELi5EEvPKDF16_S1_PK15HIP_vector_typeIfLj4EEPDF16_S6_S6_Pf
		.amdhsa_group_segment_fixed_size 0
		.amdhsa_private_segment_fixed_size 0
		.amdhsa_kernarg_size 56
		.amdhsa_user_sgpr_count 2
		.amdhsa_user_sgpr_dispatch_ptr 0
		.amdhsa_user_sgpr_queue_ptr 0
		.amdhsa_user_sgpr_kernarg_segment_ptr 1
		.amdhsa_user_sgpr_dispatch_id 0
		.amdhsa_user_sgpr_kernarg_preload_length 0
		.amdhsa_user_sgpr_kernarg_preload_offset 0
		.amdhsa_user_sgpr_private_segment_size 0
		.amdhsa_uses_dynamic_stack 0
		.amdhsa_enable_private_segment 0
		.amdhsa_system_sgpr_workgroup_id_x 1
		.amdhsa_system_sgpr_workgroup_id_y 0
		.amdhsa_system_sgpr_workgroup_id_z 0
		.amdhsa_system_sgpr_workgroup_info 0
		.amdhsa_system_vgpr_workitem_id 0
		.amdhsa_next_free_vgpr 168
		.amdhsa_next_free_sgpr 50
		.amdhsa_accum_offset 168
		.amdhsa_reserve_vcc 1
		.amdhsa_float_round_mode_32 0
		.amdhsa_float_round_mode_16_64 0
		.amdhsa_float_denorm_mode_32 3
		.amdhsa_float_denorm_mode_16_64 3
		.amdhsa_dx10_clamp 1
		.amdhsa_ieee_mode 1
		.amdhsa_fp16_overflow 0
		.amdhsa_tg_split 0
		.amdhsa_exception_fp_ieee_invalid_op 0
		.amdhsa_exception_fp_denorm_src 0
		.amdhsa_exception_fp_ieee_div_zero 0
		.amdhsa_exception_fp_ieee_overflow 0
		.amdhsa_exception_fp_ieee_underflow 0
		.amdhsa_exception_fp_ieee_inexact 0
		.amdhsa_exception_int_div_zero 0
	.end_amdhsa_kernel

amdhsa.kernels:
  - .agpr_count:     0
    .args:
      - .address_space:  global
        .offset:         0
        .size:           8
        .value_kind:     global_buffer
      - .address_space:  global
        .offset:         8
        .size:           8
        .value_kind:     global_buffer
      - .address_space:  global
        .offset:         16
        .size:           8
        .value_kind:     global_buffer
      - .address_space:  global
        .offset:         24
        .size:           8
        .value_kind:     global_buffer
      - .address_space:  global
        .offset:         32
        .size:           8
        .value_kind:     global_buffer
      - .actual_access:  write_only
        .address_space:  global
        .offset:         40
        .size:           8
        .value_kind:     global_buffer
      - .actual_access:  write_only
        .address_space:  global
        .offset:         48
        .size:           8
        .value_kind:     global_buffer
      - .actual_access:  write_only
        .address_space:  global
        .offset:         56
        .size:           8
        .value_kind:     global_buffer
      - .actual_access:  write_only
        .address_space:  global
        .offset:         64
        .size:           8
        .value_kind:     global_buffer
    .group_segment_fixed_size: 0
    .kernarg_segment_align: 8
    .kernarg_segment_size: 72
    .language:       OpenCL C
    .language_version:
      - 2
      - 0
    .max_flat_workgroup_size: 256
    .name:           _Z11prep_kernelPKfS0_S0_S0_S0_PDF16_S1_S1_P15HIP_vector_typeIfLj2EE
    .private_segment_fixed_size: 0
    .sgpr_count:     38
    .sgpr_spill_count: 0
    .symbol:         _Z11prep_kernelPKfS0_S0_S0_S0_PDF16_S1_S1_P15HIP_vector_typeIfLj2EE.kd
    .uniform_work_group_size: 1
    .uses_dynamic_stack: false
    .vgpr_count:     44
    .vgpr_spill_count: 0
    .wavefront_size: 64
  - .agpr_count:     0
    .args:
      - .address_space:  global
        .offset:         0
        .size:           8
        .value_kind:     global_buffer
      - .address_space:  global
        .offset:         8
        .size:           8
        .value_kind:     global_buffer
      - .address_space:  global
        .offset:         16
        .size:           8
        .value_kind:     global_buffer
      - .address_space:  global
        .offset:         24
        .size:           8
        .value_kind:     global_buffer
    .group_segment_fixed_size: 0
    .kernarg_segment_align: 8
    .kernarg_segment_size: 32
    .language:       OpenCL C
    .language_version:
      - 2
      - 0
    .max_flat_workgroup_size: 256
    .name:           _Z10attn64_fwdPKDF16_S0_S0_PDF16_
    .private_segment_fixed_size: 0
    .sgpr_count:     55
    .sgpr_spill_count: 0
    .symbol:         _Z10attn64_fwdPKDF16_S0_S0_PDF16_.kd
    .uniform_work_group_size: 1
    .uses_dynamic_stack: false
    .vgpr_count:     248
    .vgpr_spill_count: 0
    .wavefront_size: 64
  - .agpr_count:     0
    .args:
      - .address_space:  global
        .offset:         0
        .size:           8
        .value_kind:     global_buffer
      - .address_space:  global
        .offset:         8
        .size:           8
        .value_kind:     global_buffer
      - .actual_access:  read_only
        .address_space:  global
        .offset:         16
        .size:           8
        .value_kind:     global_buffer
      - .actual_access:  write_only
        .address_space:  global
        .offset:         24
        .size:           8
        .value_kind:     global_buffer
      - .actual_access:  write_only
        .address_space:  global
        .offset:         32
        .size:           8
        .value_kind:     global_buffer
      - .actual_access:  write_only
        .address_space:  global
        .offset:         40
        .size:           8
        .value_kind:     global_buffer
      - .actual_access:  read_only
        .address_space:  global
        .offset:         48
        .size:           8
        .value_kind:     global_buffer
    .group_segment_fixed_size: 0
    .kernarg_segment_align: 8
    .kernarg_segment_size: 56
    .language:       OpenCL C
    .language_version:
      - 2
      - 0
    .max_flat_workgroup_size: 768
    .name:           _Z11gemm_kernelILi0ELi6ELi4ELi5EEvPKDF16_S1_PK15HIP_vector_typeIfLj4EEPDF16_S6_S6_Pf
    .private_segment_fixed_size: 0
    .sgpr_count:     56
    .sgpr_spill_count: 0
    .symbol:         _Z11gemm_kernelILi0ELi6ELi4ELi5EEvPKDF16_S1_PK15HIP_vector_typeIfLj4EEPDF16_S6_S6_Pf.kd
    .uniform_work_group_size: 1
    .uses_dynamic_stack: false
    .vgpr_count:     168
    .vgpr_spill_count: 0
    .wavefront_size: 64
  - .agpr_count:     0
    .args:
      - .address_space:  global
        .offset:         0
        .size:           8
        .value_kind:     global_buffer
      - .address_space:  global
        .offset:         8
        .size:           8
        .value_kind:     global_buffer
      - .actual_access:  read_only
        .address_space:  global
        .offset:         16
        .size:           8
        .value_kind:     global_buffer
      - .actual_access:  read_only
        .address_space:  global
        .offset:         24
        .size:           8
        .value_kind:     global_buffer
      - .actual_access:  read_only
        .address_space:  global
        .offset:         32
        .size:           8
        .value_kind:     global_buffer
      - .actual_access:  read_only
        .address_space:  global
        .offset:         40
        .size:           8
        .value_kind:     global_buffer
      - .actual_access:  write_only
        .address_space:  global
        .offset:         48
        .size:           8
        .value_kind:     global_buffer
    .group_segment_fixed_size: 0
    .kernarg_segment_align: 8
    .kernarg_segment_size: 56
    .language:       OpenCL C
    .language_version:
      - 2
      - 0
    .max_flat_workgroup_size: 768
    .name:           _Z11gemm_kernelILi1ELi4ELi2ELi5EEvPKDF16_S1_PK15HIP_vector_typeIfLj4EEPDF16_S6_S6_Pf
    .private_segment_fixed_size: 0
    .sgpr_count:     19
    .sgpr_spill_count: 0
    .symbol:         _Z11gemm_kernelILi1ELi4ELi2ELi5EEvPKDF16_S1_PK15HIP_vector_typeIfLj4EEPDF16_S6_S6_Pf.kd
    .uniform_work_group_size: 1
    .uses_dynamic_stack: false
    .vgpr_count:     62
    .vgpr_spill_count: 0
    .wavefront_size: 64
